# FFN-up tile head: next tile's row-scale table entry fetched by LDS-DMA straight into its LDS slot (no VGPR round trip, no wait at the tile start)
# baseline (speedup 1.0000x reference)
; template <class Epi, bool ALIGN_EPI, bool SP2>
; __device__ __forceinline__ void gemm_phase(LAS unsigned char* lds, LAS float* tab, const Gemm g, const StaticOrder& S, const Epi& E, int wave_s) {
;     ...
;         const bool has_next = S.next(ui + 1, nxt);
;         if constexpr (Epi::NEED_RSTD) {
;             if (Epi::I8) { if (tid < 256) tab[(ui & 1) * 256 + tid] = g.ssp[(size_t)cur.pm * BM + tid]; }
;             else if (tid < 256) { const f32x4* p = (const f32x4*)(g.ssp + ((size_t)cur.pm * BM + tid) * 16); const f32x4 a = p[0], b = p[1], c = p[2], d = p[3];
;                 const float s = ((a[0] + a[1]) + (a[2] + a[3])) + ((b[0] + b[1]) + (b[2] + b[3])) + ((c[0] + c[1]) + (c[2] + c[3])) + ((d[0] + d[1]) + (d[2] + d[3]));
;                 tab[(ui & 1) * 256 + tid] = rsqrtf(s * (1.0f / D) + EPS); }
.LBB0_2074:
	s_and_saveexec_b64 s[8:9], s[6:7]
	s_cbranch_execz .LBB0_2076
	s_ashr_i32 s27, s26, 31
	s_lshl_b64 s[2:3], s[26:27], 10
	v_lshl_add_u64 v[2:3], v[208:209], 0, s[2:3]
	s_lshl_b32 s1, s0, 10
	s_and_b32 s1, s1, 0x400
	v_readfirstlane_b32 s2, v225
	s_mov_b32 s3, m0
	s_add_i32 s1, s1, s2
	s_mov_b32 m0, s1
	s_nop 0
	global_load_lds_dword v[2:3], off
	s_mov_b32 m0, s3

; template <class Epi, bool ALIGN_EPI, bool SP2>
; __device__ __forceinline__ void gemm_phase(LAS unsigned char* lds, LAS float* tab, const Gemm g, const StaticOrder& S, const Epi& E, int wave_s) {
;     ...
;         const char* nA = has_next ? (const char*)g.A + (size_t)nxt.pm * tstepA + (nxt.hs > 0 ? hstepA : 0) : cA; const char* nB = has_next ? (const char*)g.Bt + (size_t)nxt.pn * tstepB : cB;
;         const bool half = cur.hs >= 0;
;         for (int t = 0; t < nt; t += 2) {
;             const bool last = (t == nt - 2);
;             const char* a1 = cA + (size_t)(t + 1) * kstep;
;             const char* a2 = last ? nA : cA + (size_t)(t + 2) * kstep; const char* b2 = last ? nB : cB + (size_t)(t + 2) * kstep;
;             const char* a3 = a2 + kstep; const char* b3 = b2 + kstep;
;     ...
; #pragma unroll
;         for (int a = 0; a < 2; ++a)
; #pragma unroll
;             for (int b = 0; b < 2; ++b)
; #pragma unroll
;                 for (int m = 0; m < 4; ++m)
; #pragma unroll
;                     for (int n = 0; n < 2; ++n) acc[a][b][m][n] = AccV{};
.LBB0_2078:
	s_ashr_i32 s19, s18, 31
	s_lshl_b64 s[2:3], s[18:19], 18
	s_add_u32 s24, s45, s2
	s_addc_u32 s25, s46, s3
	s_and_b64 s[2:3], s[10:11], exec
	s_cselect_b32 s1, s25, s37
	s_cselect_b32 s2, s24, s36
	s_cmp_lt_i32 s66, 0
	s_cselect_b64 s[30:31], -1, 0
	s_add_u32 s34, s34, 0x20080
	s_addc_u32 s35, s35, 0
	v_mov_b32_e32 v2, v1
	v_mov_b32_e32 v3, v1
	s_add_u32 s3, s36, 0x100
	v_mov_b32_e32 v0, v1
	s_waitcnt vmcnt(1)
	v_mov_b32_e32 v84, 0
	v_mov_b64_e32 v[6:7], v[2:3]
	v_mov_b64_e32 v[14:15], v[2:3]
	v_mov_b64_e32 v[22:23], v[2:3]
	v_mov_b64_e32 v[30:31], v[2:3]
	v_mov_b64_e32 v[38:39], v[2:3]
	v_mov_b64_e32 v[46:47], v[2:3]
	v_mov_b64_e32 v[54:55], v[2:3]
	v_mov_b64_e32 v[70:71], v[2:3]
	v_mov_b64_e32 v[10:11], v[2:3]
	v_mov_b64_e32 v[18:19], v[2:3]
	v_mov_b64_e32 v[26:27], v[2:3]
	v_mov_b64_e32 v[34:35], v[2:3]
	v_mov_b64_e32 v[42:43], v[2:3]
	v_mov_b64_e32 v[50:51], v[2:3]
	v_mov_b64_e32 v[58:59], v[2:3]
	v_mov_b64_e32 v[74:75], v[2:3]
	s_addc_u32 s19, s37, 0
	s_mov_b32 s21, -2
	v_mov_b64_e32 v[4:5], v[0:1]
	v_mov_b64_e32 v[12:13], v[0:1]
	v_mov_b64_e32 v[20:21], v[0:1]
	v_mov_b64_e32 v[28:29], v[0:1]
	v_mov_b64_e32 v[36:37], v[0:1]
	v_mov_b64_e32 v[44:45], v[0:1]
	v_mov_b64_e32 v[52:53], v[0:1]
	v_mov_b64_e32 v[68:69], v[0:1]
	v_mov_b64_e32 v[8:9], v[0:1]
	v_mov_b64_e32 v[16:17], v[0:1]
	v_mov_b64_e32 v[24:25], v[0:1]
	v_mov_b64_e32 v[32:33], v[0:1]
	v_mov_b64_e32 v[40:41], v[0:1]
	v_mov_b64_e32 v[48:49], v[0:1]
	v_mov_b64_e32 v[56:57], v[0:1]
	v_mov_b64_e32 v[72:73], v[0:1]
	v_mov_b32_e32 v85, v84
	v_mov_b32_e32 v86, v84
	v_mov_b32_e32 v87, v84
	v_mov_b32_e32 v92, v84
	v_mov_b32_e32 v93, v84
	v_mov_b32_e32 v94, v84
	v_mov_b32_e32 v95, v84
	v_mov_b32_e32 v100, v84
	v_mov_b32_e32 v101, v84
	v_mov_b32_e32 v102, v84
	v_mov_b32_e32 v103, v84
	v_mov_b32_e32 v108, v84
	v_mov_b32_e32 v109, v84
	v_mov_b32_e32 v110, v84
	v_mov_b32_e32 v111, v84
	v_mov_b32_e32 v116, v84
	v_mov_b32_e32 v117, v84
	v_mov_b32_e32 v118, v84
	v_mov_b32_e32 v119, v84
	v_mov_b32_e32 v124, v84
	v_mov_b32_e32 v125, v84
	v_mov_b32_e32 v126, v84
	v_mov_b32_e32 v127, v84
	v_mov_b32_e32 v132, v84
	v_mov_b32_e32 v133, v84
	v_mov_b32_e32 v134, v84
	v_mov_b32_e32 v135, v84
	v_mov_b32_e32 v140, v84
	v_mov_b32_e32 v141, v84
	v_mov_b32_e32 v142, v84
	v_mov_b32_e32 v143, v84
	v_mov_b32_e32 v88, v84
	v_mov_b32_e32 v89, v84
	v_mov_b32_e32 v90, v84
	v_mov_b32_e32 v91, v84
	v_mov_b32_e32 v96, v84
	v_mov_b32_e32 v97, v84
	v_mov_b32_e32 v98, v84
	v_mov_b32_e32 v99, v84
	v_mov_b32_e32 v104, v84
	v_mov_b32_e32 v105, v84
	v_mov_b32_e32 v106, v84
	v_mov_b32_e32 v107, v84
	v_mov_b32_e32 v112, v84
	v_mov_b32_e32 v113, v84
	v_mov_b32_e32 v114, v84
	v_mov_b32_e32 v115, v84
	v_mov_b32_e32 v120, v84
	v_mov_b32_e32 v121, v84
	v_mov_b32_e32 v122, v84
	v_mov_b32_e32 v123, v84
	v_mov_b32_e32 v128, v84
	v_mov_b32_e32 v129, v84
	v_mov_b32_e32 v130, v84
	v_mov_b32_e32 v131, v84
	v_mov_b32_e32 v136, v84
	v_mov_b32_e32 v137, v84
	v_mov_b32_e32 v138, v84
	v_mov_b32_e32 v139, v84
	v_mov_b32_e32 v144, v84
	v_mov_b32_e32 v145, v84
	v_mov_b32_e32 v146, v84
	v_mov_b32_e32 v147, v84
	s_branch .LBB0_2080
